# dsa_tail_gemm K-loop: 48 serialized load-wait-mfma round trips replaced by a 7-deep rolling register pipeline
# baseline (speedup 1.0000x reference)
.LBB0_856:
	v_ashrrev_i32_e32 v57, 31, v56
	v_lshlrev_b64 v[2:3], 12, v[56:57]
	v_lshl_add_u64 v[60:61], v[54:55], 0, v[2:3]
	v_mov_b32_e32 v2, 0
	s_mov_b64 s[6:7], 0
	v_mov_b32_e32 v3, v2
	v_mov_b32_e32 v4, v2
	v_mov_b32_e32 v5, v2
	v_mov_b32_e32 v6, v2
	v_mov_b32_e32 v7, v2
	v_mov_b32_e32 v8, v2
	v_mov_b32_e32 v9, v2
	v_mov_b32_e32 v10, v2
	v_mov_b32_e32 v11, v2
	v_mov_b32_e32 v12, v2
	v_mov_b32_e32 v13, v2
	v_mov_b32_e32 v14, v2
	v_mov_b32_e32 v15, v2
	v_mov_b32_e32 v16, v2
	v_mov_b32_e32 v17, v2
	v_mov_b32_e32 v18, v2
	v_mov_b32_e32 v19, v2
	v_mov_b32_e32 v20, v2
	v_mov_b32_e32 v21, v2
	v_mov_b32_e32 v22, v2
	v_mov_b32_e32 v23, v2
	v_mov_b32_e32 v24, v2
	v_mov_b32_e32 v25, v2
	v_mov_b32_e32 v26, v2
	v_mov_b32_e32 v27, v2
	v_mov_b32_e32 v28, v2
	v_mov_b32_e32 v29, v2
	v_mov_b32_e32 v30, v2
	v_mov_b32_e32 v31, v2
	v_mov_b32_e32 v32, v2
	v_mov_b32_e32 v33, v2
	v_mov_b32_e32 v34, v2
	v_mov_b32_e32 v35, v2
	v_mov_b32_e32 v36, v2
	v_mov_b32_e32 v37, v2
	v_mov_b32_e32 v38, v2
	v_mov_b32_e32 v39, v2
	v_mov_b32_e32 v40, v2
	v_mov_b32_e32 v41, v2
	v_mov_b32_e32 v42, v2
	v_mov_b32_e32 v43, v2
	v_mov_b32_e32 v44, v2
	v_mov_b32_e32 v45, v2
	v_mov_b32_e32 v46, v2
	v_mov_b32_e32 v47, v2
	v_mov_b32_e32 v48, v2
	v_mov_b32_e32 v49, v2
	v_add_co_u32_e32 v76, vcc, 0x1000000, v52
	s_nop 1
	v_addc_co_u32_e32 v77, vcc, 0, v53, vcc
	v_add_co_u32_e32 v78, vcc, 0x1020000, v52
	s_nop 1
	v_addc_co_u32_e32 v79, vcc, 0, v53, vcc
	v_add_co_u32_e32 v80, vcc, 0x1040000, v52
	s_nop 1
	v_addc_co_u32_e32 v81, vcc, 0, v53, vcc
	global_load_dwordx4 v[84:87], v[60:61], off offset:-64
	global_load_dwordx4 v[88:91], v[76:77], off
	global_load_dwordx4 v[92:95], v[78:79], off
	global_load_dwordx4 v[96:99], v[80:81], off
	global_load_dwordx4 v[100:103], v[60:61], off offset:-32
	global_load_dwordx4 v[104:107], v[76:77], off offset:32
	global_load_dwordx4 v[108:111], v[78:79], off offset:32
	global_load_dwordx4 v[112:115], v[80:81], off offset:32
	global_load_dwordx4 v[116:119], v[60:61], off
	global_load_dwordx4 v[120:123], v[76:77], off offset:64
	global_load_dwordx4 v[124:127], v[78:79], off offset:64
	global_load_dwordx4 v[128:131], v[80:81], off offset:64
	global_load_dwordx4 v[132:135], v[60:61], off offset:32
	global_load_dwordx4 v[136:139], v[76:77], off offset:96
	global_load_dwordx4 v[140:143], v[78:79], off offset:96
	global_load_dwordx4 v[144:147], v[80:81], off offset:96
	global_load_dwordx4 v[148:151], v[60:61], off offset:64
	global_load_dwordx4 v[152:155], v[76:77], off offset:128
	global_load_dwordx4 v[156:159], v[78:79], off offset:128
	global_load_dwordx4 v[160:163], v[80:81], off offset:128
	global_load_dwordx4 v[164:167], v[60:61], off offset:96
	global_load_dwordx4 v[168:171], v[76:77], off offset:160
	global_load_dwordx4 v[172:175], v[78:79], off offset:160
	global_load_dwordx4 v[176:179], v[80:81], off offset:160
	global_load_dwordx4 v[180:183], v[60:61], off offset:128
	global_load_dwordx4 v[184:187], v[76:77], off offset:192
	global_load_dwordx4 v[188:191], v[78:79], off offset:192
	global_load_dwordx4 v[192:195], v[80:81], off offset:192
	s_waitcnt vmcnt(24)
	v_mfma_f32_32x32x16_bf16 v[34:49], v[84:87], v[88:91], v[34:49]
	v_mfma_f32_32x32x16_bf16 v[18:33], v[84:87], v[92:95], v[18:33]
	v_mfma_f32_32x32x16_bf16 v[2:17], v[84:87], v[96:99], v[2:17]
	global_load_dwordx4 v[84:87], v[60:61], off offset:160
	global_load_dwordx4 v[88:91], v[76:77], off offset:224
	global_load_dwordx4 v[92:95], v[78:79], off offset:224
	global_load_dwordx4 v[96:99], v[80:81], off offset:224
	s_waitcnt vmcnt(24)
	v_mfma_f32_32x32x16_bf16 v[34:49], v[100:103], v[104:107], v[34:49]
	v_mfma_f32_32x32x16_bf16 v[18:33], v[100:103], v[108:111], v[18:33]
	v_mfma_f32_32x32x16_bf16 v[2:17], v[100:103], v[112:115], v[2:17]
	global_load_dwordx4 v[100:103], v[60:61], off offset:192
	global_load_dwordx4 v[104:107], v[76:77], off offset:256
	global_load_dwordx4 v[108:111], v[78:79], off offset:256
	global_load_dwordx4 v[112:115], v[80:81], off offset:256
	s_waitcnt vmcnt(24)
	v_mfma_f32_32x32x16_bf16 v[34:49], v[116:119], v[120:123], v[34:49]
	v_mfma_f32_32x32x16_bf16 v[18:33], v[116:119], v[124:127], v[18:33]
	v_mfma_f32_32x32x16_bf16 v[2:17], v[116:119], v[128:131], v[2:17]
	global_load_dwordx4 v[116:119], v[60:61], off offset:224
	global_load_dwordx4 v[120:123], v[76:77], off offset:288
	global_load_dwordx4 v[124:127], v[78:79], off offset:288
	global_load_dwordx4 v[128:131], v[80:81], off offset:288
	s_waitcnt vmcnt(24)
	v_mfma_f32_32x32x16_bf16 v[34:49], v[132:135], v[136:139], v[34:49]
	v_mfma_f32_32x32x16_bf16 v[18:33], v[132:135], v[140:143], v[18:33]
	v_mfma_f32_32x32x16_bf16 v[2:17], v[132:135], v[144:147], v[2:17]
	global_load_dwordx4 v[132:135], v[60:61], off offset:256
	global_load_dwordx4 v[136:139], v[76:77], off offset:320
	global_load_dwordx4 v[140:143], v[78:79], off offset:320
	global_load_dwordx4 v[144:147], v[80:81], off offset:320
	s_waitcnt vmcnt(24)
	v_mfma_f32_32x32x16_bf16 v[34:49], v[148:151], v[152:155], v[34:49]
	v_mfma_f32_32x32x16_bf16 v[18:33], v[148:151], v[156:159], v[18:33]
	v_mfma_f32_32x32x16_bf16 v[2:17], v[148:151], v[160:163], v[2:17]
	global_load_dwordx4 v[148:151], v[60:61], off offset:288
	global_load_dwordx4 v[152:155], v[76:77], off offset:352
	global_load_dwordx4 v[156:159], v[78:79], off offset:352
	global_load_dwordx4 v[160:163], v[80:81], off offset:352
	s_waitcnt vmcnt(24)
	v_mfma_f32_32x32x16_bf16 v[34:49], v[164:167], v[168:171], v[34:49]
	v_mfma_f32_32x32x16_bf16 v[18:33], v[164:167], v[172:175], v[18:33]
	v_mfma_f32_32x32x16_bf16 v[2:17], v[164:167], v[176:179], v[2:17]
	global_load_dwordx4 v[164:167], v[60:61], off offset:320
	global_load_dwordx4 v[168:171], v[76:77], off offset:384
	global_load_dwordx4 v[172:175], v[78:79], off offset:384
	global_load_dwordx4 v[176:179], v[80:81], off offset:384
	s_waitcnt vmcnt(24)
	v_mfma_f32_32x32x16_bf16 v[34:49], v[180:183], v[184:187], v[34:49]
	v_mfma_f32_32x32x16_bf16 v[18:33], v[180:183], v[188:191], v[18:33]
	v_mfma_f32_32x32x16_bf16 v[2:17], v[180:183], v[192:195], v[2:17]
	global_load_dwordx4 v[180:183], v[60:61], off offset:352
	global_load_dwordx4 v[184:187], v[76:77], off offset:416
	global_load_dwordx4 v[188:191], v[78:79], off offset:416
	global_load_dwordx4 v[192:195], v[80:81], off offset:416
	s_waitcnt vmcnt(24)
	v_mfma_f32_32x32x16_bf16 v[34:49], v[84:87], v[88:91], v[34:49]
	v_mfma_f32_32x32x16_bf16 v[18:33], v[84:87], v[92:95], v[18:33]
	v_mfma_f32_32x32x16_bf16 v[2:17], v[84:87], v[96:99], v[2:17]
	global_load_dwordx4 v[84:87], v[60:61], off offset:384
	global_load_dwordx4 v[88:91], v[76:77], off offset:448
	global_load_dwordx4 v[92:95], v[78:79], off offset:448
	global_load_dwordx4 v[96:99], v[80:81], off offset:448
	s_waitcnt vmcnt(24)
	v_mfma_f32_32x32x16_bf16 v[34:49], v[100:103], v[104:107], v[34:49]
	v_mfma_f32_32x32x16_bf16 v[18:33], v[100:103], v[108:111], v[18:33]
	v_mfma_f32_32x32x16_bf16 v[2:17], v[100:103], v[112:115], v[2:17]
	global_load_dwordx4 v[100:103], v[60:61], off offset:416
	global_load_dwordx4 v[104:107], v[76:77], off offset:480
	global_load_dwordx4 v[108:111], v[78:79], off offset:480
	global_load_dwordx4 v[112:115], v[80:81], off offset:480
	s_waitcnt vmcnt(24)
	v_mfma_f32_32x32x16_bf16 v[34:49], v[116:119], v[120:123], v[34:49]
	v_mfma_f32_32x32x16_bf16 v[18:33], v[116:119], v[124:127], v[18:33]
	v_mfma_f32_32x32x16_bf16 v[2:17], v[116:119], v[128:131], v[2:17]
	s_waitcnt vmcnt(20)
	v_mfma_f32_32x32x16_bf16 v[34:49], v[132:135], v[136:139], v[34:49]
	v_mfma_f32_32x32x16_bf16 v[18:33], v[132:135], v[140:143], v[18:33]
	v_mfma_f32_32x32x16_bf16 v[2:17], v[132:135], v[144:147], v[2:17]
	s_waitcnt vmcnt(16)
	v_mfma_f32_32x32x16_bf16 v[34:49], v[148:151], v[152:155], v[34:49]
	v_mfma_f32_32x32x16_bf16 v[18:33], v[148:151], v[156:159], v[18:33]
	v_mfma_f32_32x32x16_bf16 v[2:17], v[148:151], v[160:163], v[2:17]
	s_waitcnt vmcnt(12)
	v_mfma_f32_32x32x16_bf16 v[34:49], v[164:167], v[168:171], v[34:49]
	v_mfma_f32_32x32x16_bf16 v[18:33], v[164:167], v[172:175], v[18:33]
	v_mfma_f32_32x32x16_bf16 v[2:17], v[164:167], v[176:179], v[2:17]
	s_waitcnt vmcnt(8)
	v_mfma_f32_32x32x16_bf16 v[34:49], v[180:183], v[184:187], v[34:49]
	v_mfma_f32_32x32x16_bf16 v[18:33], v[180:183], v[188:191], v[18:33]
	v_mfma_f32_32x32x16_bf16 v[2:17], v[180:183], v[192:195], v[2:17]
	s_waitcnt vmcnt(4)
	v_mfma_f32_32x32x16_bf16 v[34:49], v[84:87], v[88:91], v[34:49]
	v_mfma_f32_32x32x16_bf16 v[18:33], v[84:87], v[92:95], v[18:33]
	v_mfma_f32_32x32x16_bf16 v[2:17], v[84:87], v[96:99], v[2:17]
	s_waitcnt vmcnt(0)
	v_mfma_f32_32x32x16_bf16 v[34:49], v[100:103], v[104:107], v[34:49]
	v_mfma_f32_32x32x16_bf16 v[18:33], v[100:103], v[108:111], v[18:33]
	v_mfma_f32_32x32x16_bf16 v[2:17], v[100:103], v[112:115], v[2:17]
	s_nop 7
	s_nop 7
	ds_write2_b32 v51, v34, v18 offset1:32
	ds_write2_b32 v51, v36, v20 offset0:192 offset1:224
	v_add_u32_e32 v18, 0xc00, v51
	ds_write2_b32 v18, v38, v22 offset1:32
	ds_write2_b32 v18, v40, v24 offset0:192 offset1:224
	v_add_u32_e32 v20, 0x1800, v51
	v_add_u32_e32 v22, 0x2400, v51
	ds_write2_b32 v20, v42, v26 offset1:32
	ds_write2_b32 v20, v44, v28 offset0:192 offset1:224
	ds_write2_b32 v22, v46, v30 offset1:32
	ds_write2_b32 v22, v48, v32 offset0:192 offset1:224
	ds_write2_b32 v51, v2, v35 offset0:64 offset1:96
	ds_write2_b32 v51, v19, v3 offset0:128 offset1:160
	v_add_u32_e32 v2, 0x400, v51
	ds_write2_b32 v2, v4, v37 offset1:32
	ds_write2_b32 v2, v21, v5 offset0:64 offset1:96
	ds_write2_b32 v18, v6, v39 offset0:64 offset1:96
	ds_write2_b32 v18, v23, v7 offset0:128 offset1:160
	v_add_u32_e32 v2, 0x1000, v51
	ds_write2_b32 v2, v8, v41 offset1:32
	ds_write2_b32 v2, v25, v9 offset0:64 offset1:96
	ds_write2_b32 v20, v10, v43 offset0:64 offset1:96
	ds_write2_b32 v20, v27, v11 offset0:128 offset1:160
	v_add_u32_e32 v2, 0x1c00, v51
	ds_write2_b32 v2, v12, v45 offset1:32
	ds_write2_b32 v2, v29, v13 offset0:64 offset1:96
	ds_write2_b32 v22, v14, v47 offset0:64 offset1:96
	ds_write2_b32 v22, v31, v15 offset0:128 offset1:160
	v_add_u32_e32 v2, 0x2800, v51
	ds_write2_b32 v2, v16, v49 offset1:32
	ds_write2_b32 v2, v33, v17 offset0:64 offset1:96
	s_waitcnt lgkmcnt(0)
	s_barrier
	s_and_saveexec_b64 s[6:7], s[0:1]
	s_cbranch_execz .LBB0_855
	s_mov_b64 s[28:29], 0
	v_mov_b64_e32 v[2:3], v[58:59]
	v_mov_b32_e32 v4, v50
